# v17
# speedup vs baseline: 1.0134x; 1.0134x over previous
.LBB2_35:
	s_lshl_b32 s28, s27, 2
	v_add_u32_e32 v79, s28, v3
	v_lshl_add_u32 v79, v79, 2, v2
	ds_read_b32 v80, v79 offset:15360
	ds_read_b32 v81, v79 offset:15364
	ds_read_b32 v82, v79 offset:15368
	ds_read_b32 v79, v79 offset:15372
	v_cmp_lt_i32_e32 vcc, s28, v5
	s_or_b32 s29, s28, 1
	s_or_b32 s30, s28, 2
	s_waitcnt lgkmcnt(0)
	v_cndmask_b32_e32 v87, v9, v80, vcc
	v_cmp_lt_i32_e32 vcc, s29, v5
	s_or_b32 s31, s28, 3
	s_nop 0
	v_cndmask_b32_e32 v88, v9, v81, vcc
	v_cmp_lt_i32_e32 vcc, s30, v5
	v_lshl_or_b32 v83, v87, 7, v66
	v_lshlrev_b32_e32 v87, 2, v87
	v_cndmask_b32_e32 v89, v9, v82, vcc
	v_cmp_lt_i32_e32 vcc, s31, v5
	v_lshl_or_b32 v84, v88, 7, v66
	v_lshl_or_b32 v85, v89, 7, v66
	v_cndmask_b32_e32 v90, v9, v79, vcc
	v_lshl_or_b32 v86, v90, 7, v66
	v_lshlrev_b32_e32 v88, 2, v88
	v_lshlrev_b32_e32 v89, 2, v89
	v_lshlrev_b32_e32 v90, 2, v90
	s_waitcnt vmcnt(10)
	v_cvt_pk_f16_f32 v10, v61, v62
	v_perm_b32 v11, v40, v38, s23
	v_dot2c_f32_f16_e32 v60, v11, v10
	v_perm_b32 v11, v40, v38, s24
	v_dot2c_f32_f16_e32 v42, v11, v10
	v_perm_b32 v11, v40, v38, s25
	v_dot2c_f32_f16_e32 v43, v11, v10
	v_perm_b32 v11, v40, v38, s26
	v_dot2c_f32_f16_e32 v36, v11, v10
	v_perm_b32 v11, v41, v39, s23
	v_dot2c_f32_f16_e32 v37, v11, v10
	v_perm_b32 v11, v41, v39, s24
	v_dot2c_f32_f16_e32 v30, v11, v10
	v_perm_b32 v11, v41, v39, s25
	v_dot2c_f32_f16_e32 v31, v11, v10
	v_perm_b32 v11, v41, v39, s26
	v_dot2c_f32_f16_e32 v53, v11, v10
	v_dot2c_f32_f16_e32 v45, 0x3c003c00, v10
	s_waitcnt vmcnt(8)
	v_cvt_pk_f16_f32 v10, v58, v59
	v_perm_b32 v11, v34, v32, s23
	v_dot2c_f32_f16_e32 v60, v11, v10
	v_perm_b32 v11, v34, v32, s24
	v_dot2c_f32_f16_e32 v42, v11, v10
	v_perm_b32 v11, v34, v32, s25
	v_dot2c_f32_f16_e32 v43, v11, v10
	v_perm_b32 v11, v34, v32, s26
	v_dot2c_f32_f16_e32 v36, v11, v10
	v_perm_b32 v11, v35, v33, s23
	v_dot2c_f32_f16_e32 v37, v11, v10
	v_perm_b32 v11, v35, v33, s24
	v_dot2c_f32_f16_e32 v30, v11, v10
	v_perm_b32 v11, v35, v33, s25
	v_dot2c_f32_f16_e32 v31, v11, v10
	v_perm_b32 v11, v35, v33, s26
	s_add_i32 s5, s5, 1
	v_dot2c_f32_f16_e32 v53, v11, v10
	s_cmp_lg_u32 s5, s4
	v_dot2c_f32_f16_e32 v45, 0x3c003c00, v10
	s_cbranch_scc1 .LBB2_43
	v_cmp_gt_i32_e32 vcc, 15, v18
	s_and_saveexec_b64 s[4:5], vcc
	s_cbranch_execz .LBB2_38
	v_max_i32_e32 v10, 1, v44
	v_cvt_f32_u32_e32 v10, v10
	v_rcp_iflag_f32_e32 v44, v10
	s_nop 0
	v_pk_mul_f32 v[10:11], v[44:45], s[2:3]
	s_nop 0
	v_mul_f32_e32 v14, 0x4b800000, v10
	v_pk_mul_f32 v[16:17], v[10:11], v[10:11] op_sel:[0,1] op_sel_hi:[1,0]
	s_nop 0
	v_fma_mixlo_f16 v15, v60, v14, v16
	v_pk_fma_f32 v[10:11], v[42:43], v[14:15], v[16:17] op_sel_hi:[1,0,0]
	v_pk_fma_f32 v[12:13], v[36:37], v[14:15], v[16:17] op_sel_hi:[1,0,0]
	v_pk_fma_f32 v[30:31], v[30:31], v[14:15], v[16:17] op_sel_hi:[1,0,0]
	v_cvt_pk_f16_f32 v11, v10, v11
	v_cvt_pk_f16_f32 v12, v12, v13
	v_cvt_pk_f16_f32 v13, v30, v31
	v_pack_b32_f16 v10, v15, v11
	v_alignbit_b32 v11, v12, v11, 16
	v_alignbit_b32 v12, v13, v12, 16
	v_lshrrev_b32_e32 v13, 16, v13
	v_fma_mixhi_f16 v13, v53, v14, v16
	v_add_u32_e32 v14, v18, v77
	v_xor_b32_e32 v15, v14, v0
	v_lshlrev_b32_e32 v15, 4, v15
	v_and_b32_e32 v15, 0xf0, v15
	v_lshl_or_b32 v14, v14, 8, v15
	ds_write_b128 v14, v[10:13]

.LBB2_43:
	s_add_i32 s27, s27, 1
	global_load_dwordx2 v[38:39], v83, s[10:11]
	global_load_dwordx2 v[40:41], v84, s[10:11]
	global_load_dwordx2 v[32:33], v85, s[10:11]
	global_load_dwordx2 v[34:35], v86, s[10:11]
	global_load_dword v61, v87, s[12:13]
	global_load_dword v62, v88, s[12:13]
	global_load_dword v58, v89, s[12:13]
	global_load_dword v59, v90, s[12:13]
	s_cmp_lg_u32 s27, s21
	s_cbranch_scc1 .LBB2_49
	s_cmp_eq_u32 s20, 0
	s_cbranch_scc1 .LBB2_47
	s_add_i32 s27, s20, 1
	s_mov_b32 s20, 2
	s_cmp_eq_u32 s27, 2
	v_mov_b32_e32 v3, v7
	v_mov_b32_e32 v5, v51
	s_mov_b32 s21, s16
	s_cbranch_scc1 .LBB2_48
	s_cmp_eq_u32 s27, 3
	s_cselect_b64 vcc, -1, 0
	s_and_b64 s[20:21], vcc, exec
	v_cndmask_b32_e32 v5, 0, v52, vcc
	s_cselect_b32 s21, s6, 0x7fffffff
	s_mov_b32 s20, s27
	v_mov_b32_e32 v3, v8
	s_branch .LBB2_48

.LBB2_49:
	s_lshl_b32 s28, s27, 2
	v_add_u32_e32 v79, s28, v3
	v_lshl_add_u32 v79, v79, 2, v2
	ds_read_b32 v80, v79 offset:15360
	ds_read_b32 v81, v79 offset:15364
	ds_read_b32 v82, v79 offset:15368
	ds_read_b32 v79, v79 offset:15372
	v_cmp_lt_i32_e32 vcc, s28, v5
	s_or_b32 s29, s28, 1
	s_or_b32 s30, s28, 2
	s_waitcnt lgkmcnt(0)
	v_cndmask_b32_e32 v87, v9, v80, vcc
	v_cmp_lt_i32_e32 vcc, s29, v5
	s_or_b32 s31, s28, 3
	s_nop 0
	v_cndmask_b32_e32 v88, v9, v81, vcc
	v_cmp_lt_i32_e32 vcc, s30, v5
	v_lshl_or_b32 v83, v87, 7, v66
	v_lshlrev_b32_e32 v87, 2, v87
	v_cndmask_b32_e32 v89, v9, v82, vcc
	v_cmp_lt_i32_e32 vcc, s31, v5
	v_lshl_or_b32 v84, v88, 7, v66
	v_lshl_or_b32 v85, v89, 7, v66
	v_cndmask_b32_e32 v90, v9, v79, vcc
	v_lshl_or_b32 v86, v90, 7, v66
	v_lshlrev_b32_e32 v88, 2, v88
	v_lshlrev_b32_e32 v89, 2, v89
	v_lshlrev_b32_e32 v90, 2, v90
	s_waitcnt vmcnt(10)
	v_cvt_pk_f16_f32 v10, v56, v57
	v_perm_b32 v11, v28, v26, s23
	v_dot2c_f32_f16_e32 v60, v11, v10
	v_perm_b32 v11, v28, v26, s24
	v_dot2c_f32_f16_e32 v42, v11, v10
	v_perm_b32 v11, v28, v26, s25
	v_dot2c_f32_f16_e32 v43, v11, v10
	v_perm_b32 v11, v28, v26, s26
	v_dot2c_f32_f16_e32 v36, v11, v10
	v_perm_b32 v11, v29, v27, s23
	v_dot2c_f32_f16_e32 v37, v11, v10
	v_perm_b32 v11, v29, v27, s24
	v_dot2c_f32_f16_e32 v30, v11, v10
	v_perm_b32 v11, v29, v27, s25
	v_dot2c_f32_f16_e32 v31, v11, v10
	v_perm_b32 v11, v29, v27, s26
	v_dot2c_f32_f16_e32 v53, v11, v10
	v_dot2c_f32_f16_e32 v45, 0x3c003c00, v10
	s_waitcnt vmcnt(8)
	v_cvt_pk_f16_f32 v10, v54, v55
	v_perm_b32 v11, v24, v22, s23
	v_dot2c_f32_f16_e32 v60, v11, v10
	v_perm_b32 v11, v24, v22, s24
	v_dot2c_f32_f16_e32 v42, v11, v10
	v_perm_b32 v11, v24, v22, s25
	v_dot2c_f32_f16_e32 v43, v11, v10
	v_perm_b32 v11, v24, v22, s26
	v_dot2c_f32_f16_e32 v36, v11, v10
	v_perm_b32 v11, v25, v23, s23
	v_dot2c_f32_f16_e32 v37, v11, v10
	v_perm_b32 v11, v25, v23, s24
	v_dot2c_f32_f16_e32 v30, v11, v10
	v_perm_b32 v11, v25, v23, s25
	v_dot2c_f32_f16_e32 v31, v11, v10
	v_perm_b32 v11, v25, v23, s26
	s_add_i32 s5, s5, 1
	v_dot2c_f32_f16_e32 v53, v11, v10
	s_cmp_lg_u32 s5, s4
	v_dot2c_f32_f16_e32 v45, 0x3c003c00, v10
	s_cbranch_scc1 .LBB2_57
	v_cmp_gt_i32_e32 vcc, 15, v18
	s_and_saveexec_b64 s[4:5], vcc
	s_cbranch_execz .LBB2_52
	v_max_i32_e32 v10, 1, v44
	v_cvt_f32_u32_e32 v10, v10
	v_rcp_iflag_f32_e32 v44, v10
	s_nop 0
	v_pk_mul_f32 v[10:11], v[44:45], s[2:3]
	s_nop 0
	v_mul_f32_e32 v14, 0x4b800000, v10
	v_pk_mul_f32 v[16:17], v[10:11], v[10:11] op_sel:[0,1] op_sel_hi:[1,0]
	s_nop 0
	v_fma_mixlo_f16 v15, v60, v14, v16
	v_pk_fma_f32 v[10:11], v[42:43], v[14:15], v[16:17] op_sel_hi:[1,0,0]
	v_pk_fma_f32 v[12:13], v[36:37], v[14:15], v[16:17] op_sel_hi:[1,0,0]
	v_pk_fma_f32 v[22:23], v[30:31], v[14:15], v[16:17] op_sel_hi:[1,0,0]
	v_cvt_pk_f16_f32 v11, v10, v11
	v_cvt_pk_f16_f32 v12, v12, v13
	v_cvt_pk_f16_f32 v13, v22, v23
	v_pack_b32_f16 v10, v15, v11
	v_alignbit_b32 v11, v12, v11, 16
	v_alignbit_b32 v12, v13, v12, 16
	v_lshrrev_b32_e32 v13, 16, v13
	v_fma_mixhi_f16 v13, v53, v14, v16
	v_add_u32_e32 v14, v18, v77
	v_xor_b32_e32 v15, v14, v0
	v_lshlrev_b32_e32 v15, 4, v15
	v_and_b32_e32 v15, 0xf0, v15
	v_lshl_or_b32 v14, v14, 8, v15
	ds_write_b128 v14, v[10:13]

.LBB2_57:
	s_add_i32 s27, s27, 1
	global_load_dwordx2 v[26:27], v83, s[10:11]
	global_load_dwordx2 v[28:29], v84, s[10:11]
	global_load_dwordx2 v[22:23], v85, s[10:11]
	global_load_dwordx2 v[24:25], v86, s[10:11]
	global_load_dword v56, v87, s[12:13]
	global_load_dword v57, v88, s[12:13]
	global_load_dword v54, v89, s[12:13]
	global_load_dword v55, v90, s[12:13]
	s_cmp_lg_u32 s27, s21
	s_cbranch_scc1 .LBB2_34
	s_cmp_eq_u32 s20, 0
	s_cbranch_scc1 .LBB2_32
	s_add_i32 s27, s20, 1
	s_mov_b32 s20, 2
	s_cmp_eq_u32 s27, 2
	v_mov_b32_e32 v3, v7
	v_mov_b32_e32 v5, v51
	s_mov_b32 s21, s16
	s_cbranch_scc1 .LBB2_33
	s_cmp_eq_u32 s27, 3
	s_cselect_b64 vcc, -1, 0
	s_and_b64 s[20:21], vcc, exec
	v_cndmask_b32_e32 v5, 0, v52, vcc
	s_cselect_b32 s21, s6, 0x7fffffff
	s_mov_b32 s20, s27
	v_mov_b32_e32 v3, v8
	s_branch .LBB2_33

.LBB3_33:
	s_lshl_b32 s26, s25, 2
	v_add_u32_e32 v82, s26, v3
	v_lshl_add_u32 v82, v82, 2, v2
	ds_read_b32 v83, v82 offset:15360
	ds_read_b32 v84, v82 offset:15364
	ds_read_b32 v85, v82 offset:15368
	ds_read_b32 v82, v82 offset:15372
	v_cmp_lt_i32_e32 vcc, s26, v5
	s_or_b32 s28, s26, 1
	s_or_b32 s29, s26, 2
	s_waitcnt lgkmcnt(0)
	v_cndmask_b32_e32 v87, v8, v83, vcc
	v_cmp_lt_i32_e32 vcc, s28, v5
	s_or_b32 s30, s26, 3
	s_nop 0
	v_cndmask_b32_e32 v88, v8, v84, vcc
	v_cmp_lt_i32_e32 vcc, s29, v5
	v_lshl_or_b32 v79, v87, 7, v78
	v_lshlrev_b32_e32 v87, 2, v87
	v_cndmask_b32_e32 v89, v8, v85, vcc
	v_cmp_lt_i32_e32 vcc, s30, v5
	v_lshl_or_b32 v80, v88, 7, v78
	v_lshl_or_b32 v81, v89, 7, v78
	v_cndmask_b32_e32 v90, v8, v82, vcc
	v_lshl_or_b32 v86, v90, 7, v78
	v_lshlrev_b32_e32 v88, 2, v88
	v_lshlrev_b32_e32 v89, 2, v89
	v_lshlrev_b32_e32 v90, 2, v90
	s_waitcnt vmcnt(10)
	v_cvt_pk_f16_f32 v9, v57, v58
	v_perm_b32 v10, v40, v38, s21
	v_dot2c_f32_f16_e32 v56, v10, v9
	v_perm_b32 v10, v40, v38, s22
	v_dot2c_f32_f16_e32 v42, v10, v9
	v_perm_b32 v10, v40, v38, s23
	v_dot2c_f32_f16_e32 v43, v10, v9
	v_perm_b32 v10, v40, v38, s24
	v_dot2c_f32_f16_e32 v36, v10, v9
	v_perm_b32 v10, v41, v39, s21
	v_dot2c_f32_f16_e32 v37, v10, v9
	v_perm_b32 v10, v41, v39, s22
	v_dot2c_f32_f16_e32 v30, v10, v9
	v_perm_b32 v10, v41, v39, s23
	v_dot2c_f32_f16_e32 v31, v10, v9
	v_perm_b32 v10, v41, v39, s24
	v_dot2c_f32_f16_e32 v49, v10, v9
	s_waitcnt vmcnt(8)
	v_cvt_pk_f16_f32 v9, v54, v55
	v_perm_b32 v10, v34, v32, s21
	v_dot2c_f32_f16_e32 v56, v10, v9
	v_perm_b32 v10, v34, v32, s22
	v_dot2c_f32_f16_e32 v42, v10, v9
	v_perm_b32 v10, v34, v32, s23
	v_dot2c_f32_f16_e32 v43, v10, v9
	v_perm_b32 v10, v34, v32, s24
	v_dot2c_f32_f16_e32 v36, v10, v9
	v_perm_b32 v10, v35, v33, s21
	v_dot2c_f32_f16_e32 v37, v10, v9
	v_perm_b32 v10, v35, v33, s22
	v_dot2c_f32_f16_e32 v30, v10, v9
	v_perm_b32 v10, v35, v33, s23
	v_dot2c_f32_f16_e32 v31, v10, v9
	v_perm_b32 v10, v35, v33, s24
	s_add_i32 s5, s5, 1
	v_dot2c_f32_f16_e32 v49, v10, v9
	s_cmp_lg_u32 s5, s4
	s_cbranch_scc1 .LBB3_41
	v_cmp_gt_i32_e32 vcc, 15, v18
	s_and_saveexec_b64 s[4:5], vcc
	s_cbranch_execz .LBB3_36
	v_max_i32_e32 v9, 1, v44
	v_cvt_f32_u32_e32 v9, v9
	v_rcp_iflag_f32_e32 v44, v9
	s_nop 0
	v_pk_mul_f32 v[10:11], v[44:45], s[2:3]
	s_nop 0
	v_mul_f32_e32 v14, 0x4b800000, v10
	v_pk_mul_f32 v[16:17], v[10:11], v[10:11] op_sel:[0,1] op_sel_hi:[1,0]
	s_nop 0
	v_pk_fma_f32 v[10:11], v[42:43], v[14:15], v[16:17] op_sel_hi:[1,0,0]
	v_fma_mixlo_f16 v9, v56, v14, v16
	v_pk_fma_f32 v[12:13], v[36:37], v[14:15], v[16:17] op_sel_hi:[1,0,0]
	v_pk_fma_f32 v[30:31], v[30:31], v[14:15], v[16:17] op_sel_hi:[1,0,0]
	v_cvt_pk_f16_f32 v11, v10, v11
	v_cvt_pk_f16_f32 v12, v12, v13
	v_pack_b32_f16 v10, v9, v11
	v_cvt_pk_f16_f32 v9, v30, v31
	v_alignbit_b32 v11, v12, v11, 16
	v_alignbit_b32 v12, v9, v12, 16
	v_lshrrev_b32_e32 v13, 16, v9
	v_add_u32_e32 v9, v18, v75
	v_fma_mixhi_f16 v13, v49, v14, v16
	v_xor_b32_e32 v14, v9, v0
	v_lshlrev_b32_e32 v14, 4, v14
	v_and_b32_e32 v14, 0xf0, v14
	v_lshl_or_b32 v9, v9, 8, v14
	ds_write_b128 v9, v[10:13]

.LBB3_41:
	s_add_i32 s25, s25, 1
	global_load_dwordx2 v[38:39], v79, s[10:11]
	global_load_dwordx2 v[40:41], v80, s[10:11]
	global_load_dwordx2 v[32:33], v81, s[10:11]
	global_load_dwordx2 v[34:35], v86, s[10:11]
	global_load_dword v57, v87, s[12:13]
	global_load_dword v58, v88, s[12:13]
	global_load_dword v54, v89, s[12:13]
	global_load_dword v55, v90, s[12:13]
	s_cmp_lg_u32 s25, s19
	s_cbranch_scc1 .LBB3_47
	s_cmp_eq_u32 s7, 0
	s_cbranch_scc1 .LBB3_45
	s_add_i32 s25, s7, 1
	s_mov_b32 s7, 2
	s_cmp_eq_u32 s25, 2
	v_mov_b32_e32 v3, v6
	v_mov_b32_e32 v5, v47
	s_mov_b32 s19, s15
	s_cbranch_scc1 .LBB3_46
	s_cmp_eq_u32 s25, 3
	s_cselect_b64 vcc, -1, 0
	s_and_b64 s[26:27], vcc, exec
	v_cndmask_b32_e32 v5, 0, v48, vcc
	s_cselect_b32 s19, s6, 0x7fffffff
	s_mov_b32 s7, s25
	v_mov_b32_e32 v3, v7
	s_branch .LBB3_46

.LBB3_47:
	s_lshl_b32 s26, s25, 2
	v_add_u32_e32 v82, s26, v3
	v_lshl_add_u32 v82, v82, 2, v2
	ds_read_b32 v83, v82 offset:15360
	ds_read_b32 v84, v82 offset:15364
	ds_read_b32 v85, v82 offset:15368
	ds_read_b32 v82, v82 offset:15372
	v_cmp_lt_i32_e32 vcc, s26, v5
	s_or_b32 s28, s26, 1
	s_or_b32 s29, s26, 2
	s_waitcnt lgkmcnt(0)
	v_cndmask_b32_e32 v87, v8, v83, vcc
	v_cmp_lt_i32_e32 vcc, s28, v5
	s_or_b32 s30, s26, 3
	s_nop 0
	v_cndmask_b32_e32 v88, v8, v84, vcc
	v_cmp_lt_i32_e32 vcc, s29, v5
	v_lshl_or_b32 v79, v87, 7, v78
	v_lshlrev_b32_e32 v87, 2, v87
	v_cndmask_b32_e32 v89, v8, v85, vcc
	v_cmp_lt_i32_e32 vcc, s30, v5
	v_lshl_or_b32 v80, v88, 7, v78
	v_lshl_or_b32 v81, v89, 7, v78
	v_cndmask_b32_e32 v90, v8, v82, vcc
	v_lshl_or_b32 v86, v90, 7, v78
	v_lshlrev_b32_e32 v88, 2, v88
	v_lshlrev_b32_e32 v89, 2, v89
	v_lshlrev_b32_e32 v90, 2, v90
	s_waitcnt vmcnt(10)
	v_cvt_pk_f16_f32 v9, v52, v53
	v_perm_b32 v10, v28, v26, s21
	v_dot2c_f32_f16_e32 v56, v10, v9
	v_perm_b32 v10, v28, v26, s22
	v_dot2c_f32_f16_e32 v42, v10, v9
	v_perm_b32 v10, v28, v26, s23
	v_dot2c_f32_f16_e32 v43, v10, v9
	v_perm_b32 v10, v28, v26, s24
	v_dot2c_f32_f16_e32 v36, v10, v9
	v_perm_b32 v10, v29, v27, s21
	v_dot2c_f32_f16_e32 v37, v10, v9
	v_perm_b32 v10, v29, v27, s22
	v_dot2c_f32_f16_e32 v30, v10, v9
	v_perm_b32 v10, v29, v27, s23
	v_dot2c_f32_f16_e32 v31, v10, v9
	v_perm_b32 v10, v29, v27, s24
	v_dot2c_f32_f16_e32 v49, v10, v9
	s_waitcnt vmcnt(8)
	v_cvt_pk_f16_f32 v9, v50, v51
	v_perm_b32 v10, v24, v22, s21
	v_dot2c_f32_f16_e32 v56, v10, v9
	v_perm_b32 v10, v24, v22, s22
	v_dot2c_f32_f16_e32 v42, v10, v9
	v_perm_b32 v10, v24, v22, s23
	v_dot2c_f32_f16_e32 v43, v10, v9
	v_perm_b32 v10, v24, v22, s24
	v_dot2c_f32_f16_e32 v36, v10, v9
	v_perm_b32 v10, v25, v23, s21
	v_dot2c_f32_f16_e32 v37, v10, v9
	v_perm_b32 v10, v25, v23, s22
	v_dot2c_f32_f16_e32 v30, v10, v9
	v_perm_b32 v10, v25, v23, s23
	v_dot2c_f32_f16_e32 v31, v10, v9
	v_perm_b32 v10, v25, v23, s24
	s_add_i32 s5, s5, 1
	v_dot2c_f32_f16_e32 v49, v10, v9
	s_cmp_lg_u32 s5, s4
	s_cbranch_scc1 .LBB3_55
	v_cmp_gt_i32_e32 vcc, 15, v18
	s_and_saveexec_b64 s[4:5], vcc
	s_cbranch_execz .LBB3_50
	v_max_i32_e32 v9, 1, v44
	v_cvt_f32_u32_e32 v9, v9
	v_rcp_iflag_f32_e32 v44, v9
	s_nop 0
	v_pk_mul_f32 v[10:11], v[44:45], s[2:3]
	s_nop 0
	v_mul_f32_e32 v14, 0x4b800000, v10
	v_pk_mul_f32 v[16:17], v[10:11], v[10:11] op_sel:[0,1] op_sel_hi:[1,0]
	s_nop 0
	v_pk_fma_f32 v[10:11], v[42:43], v[14:15], v[16:17] op_sel_hi:[1,0,0]
	v_fma_mixlo_f16 v9, v56, v14, v16
	v_pk_fma_f32 v[12:13], v[36:37], v[14:15], v[16:17] op_sel_hi:[1,0,0]
	v_pk_fma_f32 v[22:23], v[30:31], v[14:15], v[16:17] op_sel_hi:[1,0,0]
	v_cvt_pk_f16_f32 v11, v10, v11
	v_cvt_pk_f16_f32 v12, v12, v13
	v_pack_b32_f16 v10, v9, v11
	v_cvt_pk_f16_f32 v9, v22, v23
	v_alignbit_b32 v11, v12, v11, 16
	v_alignbit_b32 v12, v9, v12, 16
	v_lshrrev_b32_e32 v13, 16, v9
	v_add_u32_e32 v9, v18, v75
	v_fma_mixhi_f16 v13, v49, v14, v16
	v_xor_b32_e32 v14, v9, v0
	v_lshlrev_b32_e32 v14, 4, v14
	v_and_b32_e32 v14, 0xf0, v14
	v_lshl_or_b32 v9, v9, 8, v14
	ds_write_b128 v9, v[10:13]

.LBB3_55:
	s_add_i32 s25, s25, 1
	global_load_dwordx2 v[26:27], v79, s[10:11]
	global_load_dwordx2 v[28:29], v80, s[10:11]
	global_load_dwordx2 v[22:23], v81, s[10:11]
	global_load_dwordx2 v[24:25], v86, s[10:11]
	global_load_dword v52, v87, s[12:13]
	global_load_dword v53, v88, s[12:13]
	global_load_dword v50, v89, s[12:13]
	global_load_dword v51, v90, s[12:13]
	s_cmp_lg_u32 s25, s19
	s_cbranch_scc1 .LBB3_32
	s_cmp_eq_u32 s7, 0
	s_cbranch_scc1 .LBB3_30
	s_add_i32 s25, s7, 1
	s_mov_b32 s7, 2
	s_cmp_eq_u32 s25, 2
	v_mov_b32_e32 v3, v6
	v_mov_b32_e32 v5, v47
	s_mov_b32 s19, s15
	s_cbranch_scc1 .LBB3_31
	s_cmp_eq_u32 s25, 3
	s_cselect_b64 vcc, -1, 0
	s_and_b64 s[26:27], vcc, exec
	v_cndmask_b32_e32 v5, 0, v48, vcc
	s_cselect_b32 s19, s6, 0x7fffffff
	s_mov_b32 s7, s25
	v_mov_b32_e32 v3, v7
	s_branch .LBB3_31

amdhsa.kernels:
  - .agpr_count:     0
    .args:
      - .actual_access:  read_only
        .address_space:  global
        .offset:         0
        .size:           8
        .value_kind:     global_buffer
      - .actual_access:  read_only
        .address_space:  global
        .offset:         8
        .size:           8
        .value_kind:     global_buffer
      - .actual_access:  read_only
        .address_space:  global
        .offset:         16
        .size:           8
        .value_kind:     global_buffer
      - .actual_access:  read_only
        .address_space:  global
        .offset:         24
        .size:           8
        .value_kind:     global_buffer
      - .actual_access:  read_only
        .address_space:  global
        .offset:         32
        .size:           8
        .value_kind:     global_buffer
      - .actual_access:  read_only
        .address_space:  global
        .offset:         40
        .size:           8
        .value_kind:     global_buffer
      - .actual_access:  read_only
        .address_space:  global
        .offset:         48
        .size:           8
        .value_kind:     global_buffer
      - .actual_access:  write_only
        .address_space:  global
        .offset:         56
        .size:           8
        .value_kind:     global_buffer
      - .actual_access:  write_only
        .address_space:  global
        .offset:         64
        .size:           8
        .value_kind:     global_buffer
      - .actual_access:  write_only
        .address_space:  global
        .offset:         72
        .size:           8
        .value_kind:     global_buffer
      - .actual_access:  write_only
        .address_space:  global
        .offset:         80
        .size:           8
        .value_kind:     global_buffer
      - .actual_access:  write_only
        .address_space:  global
        .offset:         88
        .size:           8
        .value_kind:     global_buffer
      - .actual_access:  write_only
        .address_space:  global
        .offset:         96
        .size:           8
        .value_kind:     global_buffer
      - .actual_access:  write_only
        .address_space:  global
        .offset:         104
        .size:           8
        .value_kind:     global_buffer
      - .actual_access:  write_only
        .address_space:  global
        .offset:         112
        .size:           8
        .value_kind:     global_buffer
      - .actual_access:  write_only
        .address_space:  global
        .offset:         120
        .size:           8
        .value_kind:     global_buffer
      - .actual_access:  write_only
        .address_space:  global
        .offset:         128
        .size:           8
        .value_kind:     global_buffer
      - .offset:         136
        .size:           4
        .value_kind:     hidden_block_count_x
      - .offset:         140
        .size:           4
        .value_kind:     hidden_block_count_y
      - .offset:         144
        .size:           4
        .value_kind:     hidden_block_count_z
      - .offset:         148
        .size:           2
        .value_kind:     hidden_group_size_x
      - .offset:         150
        .size:           2
        .value_kind:     hidden_group_size_y
      - .offset:         152
        .size:           2
        .value_kind:     hidden_group_size_z
      - .offset:         154
        .size:           2
        .value_kind:     hidden_remainder_x
      - .offset:         156
        .size:           2
        .value_kind:     hidden_remainder_y
      - .offset:         158
        .size:           2
        .value_kind:     hidden_remainder_z
      - .offset:         176
        .size:           8
        .value_kind:     hidden_global_offset_x
      - .offset:         184
        .size:           8
        .value_kind:     hidden_global_offset_y
      - .offset:         192
        .size:           8
        .value_kind:     hidden_global_offset_z
      - .offset:         200
        .size:           2
        .value_kind:     hidden_grid_dims
    .group_segment_fixed_size: 27136
    .kernarg_segment_align: 8
    .kernarg_segment_size: 392
    .language:       OpenCL C
    .language_version:
      - 2
      - 0
    .max_flat_workgroup_size: 1024
    .name:           _Z3k_APKfPKiS2_S0_S0_S0_S0_PDF16_S3_S3_S3_PiS4_PhS5_PfS6_
    .private_segment_fixed_size: 0
    .sgpr_count:     40
    .sgpr_spill_count: 0
    .symbol:         _Z3k_APKfPKiS2_S0_S0_S0_S0_PDF16_S3_S3_S3_PiS4_PhS5_PfS6_.kd
    .uniform_work_group_size: 1
    .uses_dynamic_stack: false
    .vgpr_count:     48
    .vgpr_spill_count: 0
    .wavefront_size: 64
  - .agpr_count:     0
    .args:
      - .actual_access:  read_only
        .address_space:  global
        .offset:         0
        .size:           8
        .value_kind:     global_buffer
      - .actual_access:  read_only
        .address_space:  global
        .offset:         8
        .size:           8
        .value_kind:     global_buffer
      - .actual_access:  write_only
        .address_space:  global
        .offset:         16
        .size:           8
        .value_kind:     global_buffer
      - .actual_access:  write_only
        .address_space:  global
        .offset:         24
        .size:           8
        .value_kind:     global_buffer
      - .actual_access:  read_only
        .address_space:  global
        .offset:         32
        .size:           8
        .value_kind:     global_buffer
      - .actual_access:  read_only
        .address_space:  global
        .offset:         40
        .size:           8
        .value_kind:     global_buffer
    .group_segment_fixed_size: 27720
    .kernarg_segment_align: 8
    .kernarg_segment_size: 48
    .language:       OpenCL C
    .language_version:
      - 2
      - 0
    .max_flat_workgroup_size: 1024
    .name:           _Z3k_BPKiS0_PiS1_PKfPDF16_
    .private_segment_fixed_size: 0
    .sgpr_count:     40
    .sgpr_spill_count: 0
    .symbol:         _Z3k_BPKiS0_PiS1_PKfPDF16_.kd
    .uniform_work_group_size: 1
    .uses_dynamic_stack: false
    .vgpr_count:     60
    .vgpr_spill_count: 0
    .wavefront_size: 64
  - .agpr_count:     0
    .args:
      - .actual_access:  read_only
        .address_space:  global
        .offset:         0
        .size:           8
        .value_kind:     global_buffer
      - .actual_access:  read_only
        .address_space:  global
        .offset:         8
        .size:           8
        .value_kind:     global_buffer
      - .actual_access:  read_only
        .address_space:  global
        .offset:         16
        .size:           8
        .value_kind:     global_buffer
      - .actual_access:  read_only
        .address_space:  global
        .offset:         24
        .size:           8
        .value_kind:     global_buffer
      - .actual_access:  read_only
        .address_space:  global
        .offset:         32
        .size:           8
        .value_kind:     global_buffer
      - .actual_access:  read_only
        .address_space:  global
        .offset:         40
        .size:           8
        .value_kind:     global_buffer
      - .actual_access:  read_only
        .address_space:  global
        .offset:         48
        .size:           8
        .value_kind:     global_buffer
      - .actual_access:  write_only
        .address_space:  global
        .offset:         56
        .size:           8
        .value_kind:     global_buffer
      - .actual_access:  write_only
        .address_space:  global
        .offset:         64
        .size:           8
        .value_kind:     global_buffer
      - .actual_access:  write_only
        .address_space:  global
        .offset:         72
        .size:           8
        .value_kind:     global_buffer
    .group_segment_fixed_size: 30720
    .kernarg_segment_align: 8
    .kernarg_segment_size: 80
    .language:       OpenCL C
    .language_version:
      - 2
      - 0
    .max_flat_workgroup_size: 256
    .name:           _Z7k_layerILb1EEvPKvPKhPKfPKiS7_PKDF16_S5_PvPhPf
    .private_segment_fixed_size: 0
    .sgpr_count:     36
    .sgpr_spill_count: 0
    .symbol:         _Z7k_layerILb1EEvPKvPKhPKfPKiS7_PKDF16_S5_PvPhPf.kd
    .uniform_work_group_size: 1
    .uses_dynamic_stack: false
    .vgpr_count:     94
    .vgpr_spill_count: 0
    .wavefront_size: 64
  - .agpr_count:     0
    .args:
      - .actual_access:  read_only
        .address_space:  global
        .offset:         0
        .size:           8
        .value_kind:     global_buffer
      - .actual_access:  read_only
        .address_space:  global
        .offset:         8
        .size:           8
        .value_kind:     global_buffer
      - .actual_access:  read_only
        .address_space:  global
        .offset:         16
        .size:           8
        .value_kind:     global_buffer
      - .actual_access:  read_only
        .address_space:  global
        .offset:         24
        .size:           8
        .value_kind:     global_buffer
      - .actual_access:  read_only
        .address_space:  global
        .offset:         32
        .size:           8
        .value_kind:     global_buffer
      - .actual_access:  read_only
        .address_space:  global
        .offset:         40
        .size:           8
        .value_kind:     global_buffer
      - .actual_access:  read_only
        .address_space:  global
        .offset:         48
        .size:           8
        .value_kind:     global_buffer
      - .actual_access:  write_only
        .address_space:  global
        .offset:         56
        .size:           8
        .value_kind:     global_buffer
      - .actual_access:  read_only
        .address_space:  global
        .offset:         64
        .size:           8
        .value_kind:     global_buffer
      - .actual_access:  read_only
        .address_space:  global
        .offset:         72
        .size:           8
        .value_kind:     global_buffer
    .group_segment_fixed_size: 30720
    .kernarg_segment_align: 8
    .kernarg_segment_size: 80
    .language:       OpenCL C
    .language_version:
      - 2
      - 0
    .max_flat_workgroup_size: 256
    .name:           _Z7k_layerILb0EEvPKvPKhPKfPKiS7_PKDF16_S5_PvPhPf
    .private_segment_fixed_size: 0
    .sgpr_count:     34
    .sgpr_spill_count: 0
    .symbol:         _Z7k_layerILb0EEvPKvPKhPKfPKiS7_PKDF16_S5_PvPhPf.kd
    .uniform_work_group_size: 1
    .uses_dynamic_stack: false
    .vgpr_count:     92
    .vgpr_spill_count: 0
    .wavefront_size: 64
